# speedup vs baseline: 1.0198x; 1.0010x over previous
.LBB1_1:
	s_barrier
	s_add_i32 s42, s35, s94
	s_and_b32 s97, s42, 15
	s_lshl_b32 s98, s97, 3
	s_add_i32 s42, s42, 1
	s_and_b32 s99, s42, 15
	s_lshl_b32 s42, s99, 16
	s_add_i32 s42, s95, s42
	s_or_b32 s43, s42, 0x400
	buffer_load_dwordx4 v[146:149], v195, s[44:47], s42 offen sc1
	buffer_load_dwordx4 v[150:153], v195, s[44:47], s43 offen sc1
	s_or_b32 s43, s42, 0x800
	s_or_b32 s48, s42, 0xc00
	buffer_load_dwordx4 v[138:141], v195, s[44:47], s43 offen sc1
	buffer_load_dwordx4 v[142:145], v195, s[44:47], s48 offen sc1
	s_or_b32 s43, s42, 0x1000
	s_or_b32 s48, s42, 0x1400
	buffer_load_dwordx4 v[122:125], v195, s[44:47], s43 offen sc1
	buffer_load_dwordx4 v[126:129], v195, s[44:47], s48 offen sc1
	s_or_b32 s43, s42, 0x1800
	s_or_b32 s42, s42, 0x1c00
	buffer_load_dwordx4 v[130:133], v195, s[44:47], s43 offen sc1
	buffer_load_dwordx4 v[134:137], v195, s[44:47], s42 offen sc1
	s_add_i32 s98, s98, s52
	s_cmp_lg_u32 s98, s33
	s_cbranch_scc1 .LBB1_3
	v_cndmask_b32_e64 v2, v2, v198, s[0:1]
	v_cndmask_b32_e64 v3, v3, v198, s[2:3]
	v_cndmask_b32_e64 v4, v4, v198, s[4:5]
	v_cndmask_b32_e64 v5, v5, v198, s[6:7]
	v_cndmask_b32_e64 v6, v6, v198, s[8:9]
	v_cndmask_b32_e64 v7, v7, v198, s[10:11]
	v_cndmask_b32_e64 v8, v8, v198, s[12:13]
	v_cndmask_b32_e64 v9, v9, v198, s[14:15]
	v_cndmask_b32_e64 v10, v10, v198, s[16:17]
	v_cndmask_b32_e64 v11, v11, v198, s[18:19]
	v_cndmask_b32_e64 v12, v12, v198, s[20:21]
	v_cndmask_b32_e64 v13, v13, v198, s[22:23]
	v_cndmask_b32_e64 v14, v14, v198, s[24:25]
	v_cndmask_b32_e64 v15, v15, v198, s[26:27]
	v_cndmask_b32_e64 v16, v16, v198, s[28:29]
	v_cndmask_b32_e64 v17, v17, v198, s[30:31]
